# P7 side-job fp8 down-weight stores without the nt hint (so P8 re-reads them from the Infinity Cache)
# baseline (speedup 1.0000x reference)
; #define PG8_LAS __attribute__((address_space(3)))
;     __device__ __forceinline__ void issue(PG8_LAS unsigned char* lds0, int j, int tid, int wid) const {
;         const float* s0; unsigned char* d; addr(j, tid, s0, d);
;         __builtin_amdgcn_global_load_lds((const unsigned*)s0, (PG8_LAS unsigned*)(lds0 + stage + wid * 1024), 16, 0, 2);
;         __builtin_amdgcn_global_load_lds((const unsigned*)(s0 + ntot), (PG8_LAS unsigned*)(lds0 + stage + 8192 + wid * 1024), 16, 0, 2);
;     }
;     __device__ __forceinline__ void read(v4i_t& t0, v4i_t& t1, int tid, unsigned ldsb) const {
;         asm volatile("ds_read_b128 %0, %1" : "=&v"(t0) : "v"(ldsb + stage + 16u * (unsigned)tid) : "memory");
;         asm volatile("ds_read_b128 %0, %1" : "=&v"(t1) : "v"(ldsb + stage + 8192u + 16u * (unsigned)tid) : "memory");
;     }
;     __device__ __forceinline__ void finish(v4i_t& t0, v4i_t& t1, int j, int tid) const {
;         asm volatile("" : "+v"(t0), "+v"(t1));
;         const float* s0; unsigned char* d; addr(j, tid, s0, d);
;         const f32x4 r0 = __builtin_bit_cast(f32x4, t0) * 64.f, r1 = __builtin_bit_cast(f32x4, t1) * 64.f;
;         int w0 = 0, w1 = 0; w0 = __builtin_amdgcn_cvt_pk_fp8_f32(r0[0], r1[0], w0, false); w0 = __builtin_amdgcn_cvt_pk_fp8_f32(r0[1], r1[1], w0, true);
;         w1 = __builtin_amdgcn_cvt_pk_fp8_f32(r0[2], r1[2], w1, false); w1 = __builtin_amdgcn_cvt_pk_fp8_f32(r0[3], r1[3], w1, true);
;         typedef int v2is __attribute__((ext_vector_type(2))); __builtin_nontemporal_store((v2is){w0, w1}, (v2is*)d);
.Lp7vg_wd_a1:
	s_waitcnt lgkmcnt(0)
	s_barrier
	s_cmp_lt_i32 s98, 0
	s_cbranch_scc1 .Lp7vg_mmslow_a
	s_cmpk_gt_i32 s48, 0x7f
	s_cbranch_scc1 .Lp7vg_mmslow_a
	s_setprio 1
	s_waitcnt lgkmcnt(0)
	v_mfma_scale_f32_16x16x128_f8f6f4 v[202:205], v[26:33], v[58:65], v[202:205], v226, v226 op_sel_hi:[0,0,0]
	s_add_i32 s4, s98, s52
	s_add_i32 s4, s4, 1
	v_pk_mul_f32 v[70:71], v[70:71], s[14:15] op_sel_hi:[1,0]
	v_pk_mul_f32 v[72:73], v[72:73], s[14:15] op_sel_hi:[1,0]
	v_mfma_scale_f32_16x16x128_f8f6f4 v[198:201], v[18:25], v[58:65], v[198:201], v226, v226 op_sel_hi:[0,0,0]
	v_pk_mul_f32 v[74:75], v[74:75], s[14:15] op_sel_hi:[1,0]
	v_pk_mul_f32 v[76:77], v[76:77], s[14:15] op_sel_hi:[1,0]
	s_ashr_i32 s2, s4, 10
	s_ashr_i32 s3, s2, 31
	v_mfma_scale_f32_16x16x128_f8f6f4 v[186:189], v[26:33], v[50:57], v[186:189], v226, v226 op_sel_hi:[0,0,0]
	v_cvt_pk_fp8_f32 v70, v70, v74
	s_lshl_b32 s4, s4, 12
	s_lshl_b64 s[2:3], s[2:3], 22
	v_cvt_pk_fp8_f32 v70, v71, v75 op_sel:[0,0,1]
	v_mfma_scale_f32_16x16x128_f8f6f4 v[182:185], v[18:25], v[50:57], v[182:185], v226, v226 op_sel_hi:[0,0,0]
	s_and_b32 s4, s4, 0x3ff000
	v_readlane_b32 s5, v251, 50
	v_cvt_pk_fp8_f32 v71, v72, v76
	s_add_u32 s2, s5, s2
	v_mfma_scale_f32_16x16x128_f8f6f4 v[170:173], v[26:33], v[42:49], v[170:173], v226, v226 op_sel_hi:[0,0,0]
	v_readlane_b32 s5, v251, 51
	s_addc_u32 s3, s5, s3
	v_cvt_pk_fp8_f32 v71, v73, v77 op_sel:[0,0,1]
	s_add_u32 s2, s2, s4
	s_addc_u32 s3, s3, 0
	v_mfma_scale_f32_16x16x128_f8f6f4 v[166:169], v[18:25], v[42:49], v[166:169], v226, v226 op_sel_hi:[0,0,0]
	v_lshl_add_u64 v[68:69], s[2:3], 0, v[210:211]
	global_store_dwordx2 v[68:69], v[70:71], off
	s_add_i32 s4, s48, s53
	s_ashr_i32 s2, s4, 10
	v_mfma_scale_f32_16x16x128_f8f6f4 v[154:157], v[26:33], v[34:41], v[154:157], v226, v226 op_sel_hi:[0,0,0]
	s_ashr_i32 s3, s2, 31
	s_lshl_b64 s[2:3], s[2:3], 24
	s_lshl_b32 s4, s4, 14
	s_and_b32 s4, s4, 0xffc000
	v_mfma_scale_f32_16x16x128_f8f6f4 v[150:153], v[18:25], v[34:41], v[150:153], v226, v226 op_sel_hi:[0,0,0]
	s_setprio 0
	s_setprio 1
	s_add_u32 s2, s76, s2
	s_addc_u32 s3, s77, s3
	s_add_u32 s2, s2, s4
	s_addc_u32 s3, s3, 0
	v_mfma_scale_f32_16x16x128_f8f6f4 v[194:197], v[10:17], v[58:65], v[194:197], v226, v226 op_sel_hi:[0,0,0]
	v_lshlrev_b32_e32 v66, 2, v208
	v_lshl_add_u64 v[68:69], s[2:3], 0, v[66:67]
	v_lshl_add_u64 v[68:69], v[68:69], 0, s[16:17]
	global_load_dwordx4 v[70:73], v66, s[2:3] nt
	v_mfma_scale_f32_16x16x128_f8f6f4 v[190:193], v[2:9], v[58:65], v[190:193], v226, v226 op_sel_hi:[0,0,0]
	global_load_dwordx4 v[74:77], v[68:69], off nt
	s_mov_b32 s100, 3
	s_mov_b32 s98, s48
	s_add_i32 s48, s48, 1
	v_mfma_scale_f32_16x16x128_f8f6f4 v[178:181], v[10:17], v[50:57], v[178:181], v226, v226 op_sel_hi:[0,0,0]
	s_add_u32 s2, s42, 0xfffc0080
	s_addc_u32 s3, s43, -1
	s_cmp_eq_u32 s64, 12
	s_cselect_b32 s5, s23, s3
	s_cselect_b32 s4, s25, s2
	s_cselect_b32 s45, s35, s63
	s_cselect_b32 s44, s61, s62
	v_mfma_scale_f32_16x16x128_f8f6f4 v[174:177], v[2:9], v[50:57], v[174:177], v226, v226 op_sel_hi:[0,0,0]
	v_mfma_scale_f32_16x16x128_f8f6f4 v[162:165], v[10:17], v[42:49], v[162:165], v226, v226 op_sel_hi:[0,0,0]
	v_mfma_scale_f32_16x16x128_f8f6f4 v[158:161], v[2:9], v[42:49], v[158:161], v226, v226 op_sel_hi:[0,0,0]
	v_mfma_scale_f32_16x16x128_f8f6f4 v[146:149], v[10:17], v[34:41], v[146:149], v226, v226 op_sel_hi:[0,0,0]
	v_mfma_scale_f32_16x16x128_f8f6f4 v[142:145], v[2:9], v[34:41], v[142:145], v226, v226 op_sel_hi:[0,0,0]
	s_setprio 0
	s_branch .Lp7vg_mmjoin_a
.Lp7vg_mmslow_a:
	s_mov_b32 s100, 0
	s_cmp_lt_i32 s98, 0
	s_cbranch_scc1 .Lp7vg_nf_a
	s_add_i32 s4, s98, s52
	s_add_i32 s4, s4, 1
	v_pk_mul_f32 v[70:71], v[70:71], s[14:15] op_sel_hi:[1,0]
	v_pk_mul_f32 v[72:73], v[72:73], s[14:15] op_sel_hi:[1,0]
	v_pk_mul_f32 v[74:75], v[74:75], s[14:15] op_sel_hi:[1,0]
	v_pk_mul_f32 v[76:77], v[76:77], s[14:15] op_sel_hi:[1,0]
	s_ashr_i32 s2, s4, 10
	s_ashr_i32 s3, s2, 31
	v_cvt_pk_fp8_f32 v70, v70, v74
	s_lshl_b32 s4, s4, 12
	s_lshl_b64 s[2:3], s[2:3], 22
	v_cvt_pk_fp8_f32 v70, v71, v75 op_sel:[0,0,1]
	s_and_b32 s4, s4, 0x3ff000
	v_readlane_b32 s5, v251, 50
	v_cvt_pk_fp8_f32 v71, v72, v76
	s_add_u32 s2, s5, s2
	v_readlane_b32 s5, v251, 51
	s_addc_u32 s3, s5, s3
	v_cvt_pk_fp8_f32 v71, v73, v77 op_sel:[0,0,1]
	s_add_u32 s2, s2, s4
	s_addc_u32 s3, s3, 0
	v_lshl_add_u64 v[68:69], s[2:3], 0, v[210:211]
	global_store_dwordx2 v[68:69], v[70:71], off
	s_mov_b32 s100, 1

; #define PG8_LAS __attribute__((address_space(3)))
;     __device__ __forceinline__ void issue(PG8_LAS unsigned char* lds0, int j, int tid, int wid) const {
;         const float* s0; unsigned char* d; addr(j, tid, s0, d);
;         __builtin_amdgcn_global_load_lds((const unsigned*)s0, (PG8_LAS unsigned*)(lds0 + stage + wid * 1024), 16, 0, 2);
;         __builtin_amdgcn_global_load_lds((const unsigned*)(s0 + ntot), (PG8_LAS unsigned*)(lds0 + stage + 8192 + wid * 1024), 16, 0, 2);
;     }
;     __device__ __forceinline__ void read(v4i_t& t0, v4i_t& t1, int tid, unsigned ldsb) const {
;         asm volatile("ds_read_b128 %0, %1" : "=&v"(t0) : "v"(ldsb + stage + 16u * (unsigned)tid) : "memory");
;         asm volatile("ds_read_b128 %0, %1" : "=&v"(t1) : "v"(ldsb + stage + 8192u + 16u * (unsigned)tid) : "memory");
;     }
;     __device__ __forceinline__ void finish(v4i_t& t0, v4i_t& t1, int j, int tid) const {
;         asm volatile("" : "+v"(t0), "+v"(t1));
;         const float* s0; unsigned char* d; addr(j, tid, s0, d);
;         const f32x4 r0 = __builtin_bit_cast(f32x4, t0) * 64.f, r1 = __builtin_bit_cast(f32x4, t1) * 64.f;
;         int w0 = 0, w1 = 0; w0 = __builtin_amdgcn_cvt_pk_fp8_f32(r0[0], r1[0], w0, false); w0 = __builtin_amdgcn_cvt_pk_fp8_f32(r0[1], r1[1], w0, true);
;         w1 = __builtin_amdgcn_cvt_pk_fp8_f32(r0[2], r1[2], w1, false); w1 = __builtin_amdgcn_cvt_pk_fp8_f32(r0[3], r1[3], w1, true);
;         typedef int v2is __attribute__((ext_vector_type(2))); __builtin_nontemporal_store((v2is){w0, w1}, (v2is*)d);
.Lp7vg_wd_b1:
	s_waitcnt lgkmcnt(0)
	s_barrier
	s_cmp_lt_i32 s99, 0
	s_cbranch_scc1 .Lp7vg_mmslow_b
	s_cmpk_gt_i32 s48, 0x7f
	s_cbranch_scc1 .Lp7vg_mmslow_b
	s_setprio 1
	s_waitcnt lgkmcnt(0)
	v_mfma_scale_f32_16x16x128_f8f6f4 v[202:205], v[26:33], v[58:65], v[202:205], v226, v226 op_sel_hi:[0,0,0]
	s_add_i32 s65, s99, s52
	s_add_i32 s65, s65, 1
	v_pk_mul_f32 v[242:243], v[242:243], s[14:15] op_sel_hi:[1,0]
	v_pk_mul_f32 v[244:245], v[244:245], s[14:15] op_sel_hi:[1,0]
	v_mfma_scale_f32_16x16x128_f8f6f4 v[198:201], v[18:25], v[58:65], v[198:201], v226, v226 op_sel_hi:[0,0,0]
	v_pk_mul_f32 v[246:247], v[246:247], s[14:15] op_sel_hi:[1,0]
	v_pk_mul_f32 v[248:249], v[248:249], s[14:15] op_sel_hi:[1,0]
	s_ashr_i32 s46, s65, 10
	s_ashr_i32 s47, s46, 31
	v_mfma_scale_f32_16x16x128_f8f6f4 v[186:189], v[26:33], v[50:57], v[186:189], v226, v226 op_sel_hi:[0,0,0]
	v_cvt_pk_fp8_f32 v242, v242, v246
	s_lshl_b32 s65, s65, 12
	s_lshl_b64 s[46:47], s[46:47], 22
	v_cvt_pk_fp8_f32 v242, v243, v247 op_sel:[0,0,1]
	v_mfma_scale_f32_16x16x128_f8f6f4 v[182:185], v[18:25], v[50:57], v[182:185], v226, v226 op_sel_hi:[0,0,0]
	s_and_b32 s65, s65, 0x3ff000
	v_readlane_b32 s4, v251, 50
	v_cvt_pk_fp8_f32 v243, v244, v248
	s_add_u32 s46, s4, s46
	v_mfma_scale_f32_16x16x128_f8f6f4 v[170:173], v[26:33], v[42:49], v[170:173], v226, v226 op_sel_hi:[0,0,0]
	v_readlane_b32 s4, v251, 51
	s_addc_u32 s47, s4, s47
	v_cvt_pk_fp8_f32 v243, v245, v249 op_sel:[0,0,1]
	s_add_u32 s46, s46, s65
	s_addc_u32 s47, s47, 0
	v_mfma_scale_f32_16x16x128_f8f6f4 v[166:169], v[18:25], v[42:49], v[166:169], v226, v226 op_sel_hi:[0,0,0]
	v_lshl_add_u64 v[240:241], s[46:47], 0, v[210:211]
	global_store_dwordx2 v[240:241], v[242:243], off
	s_add_i32 s65, s48, s53
	s_ashr_i32 s46, s65, 10
	v_mfma_scale_f32_16x16x128_f8f6f4 v[154:157], v[26:33], v[34:41], v[154:157], v226, v226 op_sel_hi:[0,0,0]
	s_ashr_i32 s47, s46, 31
	s_lshl_b64 s[46:47], s[46:47], 24
	s_lshl_b32 s65, s65, 14
	s_and_b32 s65, s65, 0xffc000
	v_mfma_scale_f32_16x16x128_f8f6f4 v[150:153], v[18:25], v[34:41], v[150:153], v226, v226 op_sel_hi:[0,0,0]
	s_setprio 0
	s_setprio 1
	s_add_u32 s46, s76, s46
	s_addc_u32 s47, s77, s47
	s_add_u32 s46, s46, s65
	s_addc_u32 s47, s47, 0
	v_mfma_scale_f32_16x16x128_f8f6f4 v[194:197], v[10:17], v[58:65], v[194:197], v226, v226 op_sel_hi:[0,0,0]
	v_lshlrev_b32_e32 v66, 2, v208
	v_lshl_add_u64 v[240:241], s[46:47], 0, v[66:67]
	v_lshl_add_u64 v[240:241], v[240:241], 0, s[16:17]
	global_load_dwordx4 v[242:245], v66, s[46:47] nt
	v_mfma_scale_f32_16x16x128_f8f6f4 v[190:193], v[2:9], v[58:65], v[190:193], v226, v226 op_sel_hi:[0,0,0]
	global_load_dwordx4 v[246:249], v[240:241], off nt
	s_mov_b32 s100, 3
	s_mov_b32 s99, s48
	s_add_i32 s48, s48, 1
	v_mfma_scale_f32_16x16x128_f8f6f4 v[178:181], v[10:17], v[50:57], v[178:181], v226, v226 op_sel_hi:[0,0,0]
	s_add_u32 s46, s44, 0x84000
	s_addc_u32 s47, s45, 0
	v_mfma_scale_f32_16x16x128_f8f6f4 v[174:177], v[2:9], v[50:57], v[174:177], v226, v226 op_sel_hi:[0,0,0]
	v_mfma_scale_f32_16x16x128_f8f6f4 v[162:165], v[10:17], v[42:49], v[162:165], v226, v226 op_sel_hi:[0,0,0]
	v_mfma_scale_f32_16x16x128_f8f6f4 v[158:161], v[2:9], v[42:49], v[158:161], v226, v226 op_sel_hi:[0,0,0]
	v_mfma_scale_f32_16x16x128_f8f6f4 v[146:149], v[10:17], v[34:41], v[146:149], v226, v226 op_sel_hi:[0,0,0]
	v_mfma_scale_f32_16x16x128_f8f6f4 v[142:145], v[2:9], v[34:41], v[142:145], v226, v226 op_sel_hi:[0,0,0]
	s_setprio 0
	s_branch .Lp7vg_mmjoin_b
.Lp7vg_mmslow_b:
	s_mov_b32 s100, 0
	s_cmp_lt_i32 s99, 0
	s_cbranch_scc1 .Lp7vg_nf_b
	s_add_i32 s65, s99, s52
	s_add_i32 s65, s65, 1
	v_pk_mul_f32 v[242:243], v[242:243], s[14:15] op_sel_hi:[1,0]
	v_pk_mul_f32 v[244:245], v[244:245], s[14:15] op_sel_hi:[1,0]
	v_pk_mul_f32 v[246:247], v[246:247], s[14:15] op_sel_hi:[1,0]
	v_pk_mul_f32 v[248:249], v[248:249], s[14:15] op_sel_hi:[1,0]
	s_ashr_i32 s46, s65, 10
	s_ashr_i32 s47, s46, 31
	v_cvt_pk_fp8_f32 v242, v242, v246
	s_lshl_b32 s65, s65, 12
	s_lshl_b64 s[46:47], s[46:47], 22
	v_cvt_pk_fp8_f32 v242, v243, v247 op_sel:[0,0,1]
	s_and_b32 s65, s65, 0x3ff000
	v_readlane_b32 s4, v251, 50
	v_cvt_pk_fp8_f32 v243, v244, v248
	s_add_u32 s46, s4, s46
	v_readlane_b32 s4, v251, 51
	s_addc_u32 s47, s4, s47
	v_cvt_pk_fp8_f32 v243, v245, v249 op_sel:[0,0,1]
	s_add_u32 s46, s46, s65
	s_addc_u32 s47, s47, 0
	v_lshl_add_u64 v[240:241], s[46:47], 0, v[210:211]
	global_store_dwordx2 v[240:241], v[242:243], off
	s_mov_b32 s100, 1

;     __device__ __forceinline__ void finish(v4i_t& t0, v4i_t& t1, int j, int tid) const {
;         asm volatile("" : "+v"(t0), "+v"(t1));
;         const float* s0; unsigned char* d; addr(j, tid, s0, d);
;         const f32x4 r0 = __builtin_bit_cast(f32x4, t0) * 64.f, r1 = __builtin_bit_cast(f32x4, t1) * 64.f;
;         int w0 = 0, w1 = 0; w0 = __builtin_amdgcn_cvt_pk_fp8_f32(r0[0], r1[0], w0, false); w0 = __builtin_amdgcn_cvt_pk_fp8_f32(r0[1], r1[1], w0, true);
;         w1 = __builtin_amdgcn_cvt_pk_fp8_f32(r0[2], r1[2], w1, false); w1 = __builtin_amdgcn_cvt_pk_fp8_f32(r0[3], r1[3], w1, true);
;         typedef int v2is __attribute__((ext_vector_type(2))); __builtin_nontemporal_store((v2is){w0, w1}, (v2is*)d);
.LBB0_808:
	s_waitcnt vmcnt(0)
	v_readlane_b32 s56, v251, 54
	v_readlane_b32 s29, v251, 19
	s_barrier
	v_readlane_b32 s57, v251, 55
	s_mov_b32 s2, 0x42800000
	s_cmp_lt_i32 s98, 0
	s_cbranch_scc1 .Lp7vg_dx
	s_add_i32 s0, s98, s52
	s_add_i32 s0, s0, 1
	v_pk_mul_f32 v[70:71], v[70:71], s[2:3] op_sel_hi:[1,0]
	v_pk_mul_f32 v[72:73], v[72:73], s[2:3] op_sel_hi:[1,0]
	v_pk_mul_f32 v[74:75], v[74:75], s[2:3] op_sel_hi:[1,0]
	v_pk_mul_f32 v[76:77], v[76:77], s[2:3] op_sel_hi:[1,0]
	s_ashr_i32 s4, s0, 10
	s_ashr_i32 s5, s4, 31
	v_cvt_pk_fp8_f32 v70, v70, v74
	s_lshl_b32 s0, s0, 12
	s_lshl_b64 s[4:5], s[4:5], 22
	v_cvt_pk_fp8_f32 v70, v71, v75 op_sel:[0,0,1]
	s_and_b32 s0, s0, 0x3ff000
	v_readlane_b32 s1, v251, 50
	v_cvt_pk_fp8_f32 v71, v72, v76
	s_add_u32 s4, s1, s4
	v_readlane_b32 s1, v251, 51
	s_addc_u32 s5, s1, s5
	v_cvt_pk_fp8_f32 v71, v73, v77 op_sel:[0,0,1]
	s_add_u32 s4, s4, s0
	s_addc_u32 s5, s5, 0
	v_lshl_add_u64 v[68:69], s[4:5], 0, v[210:211]
	global_store_dwordx2 v[68:69], v[70:71], off
.Lp7vg_dx:
	s_cmp_lt_i32 s99, 0
	s_cbranch_scc1 .Lp7vg_dy
	s_add_i32 s0, s99, s52
	s_add_i32 s0, s0, 1
	v_pk_mul_f32 v[242:243], v[242:243], s[2:3] op_sel_hi:[1,0]
	v_pk_mul_f32 v[244:245], v[244:245], s[2:3] op_sel_hi:[1,0]
	v_pk_mul_f32 v[246:247], v[246:247], s[2:3] op_sel_hi:[1,0]
	v_pk_mul_f32 v[248:249], v[248:249], s[2:3] op_sel_hi:[1,0]
	s_ashr_i32 s4, s0, 10
	s_ashr_i32 s5, s4, 31
	v_cvt_pk_fp8_f32 v242, v242, v246
	s_lshl_b32 s0, s0, 12
	s_lshl_b64 s[4:5], s[4:5], 22
	v_cvt_pk_fp8_f32 v242, v243, v247 op_sel:[0,0,1]
	s_and_b32 s0, s0, 0x3ff000
	v_readlane_b32 s1, v251, 50
	v_cvt_pk_fp8_f32 v243, v244, v248
	s_add_u32 s4, s1, s4
	v_readlane_b32 s1, v251, 51
	s_addc_u32 s5, s1, s5
	v_cvt_pk_fp8_f32 v243, v245, v249 op_sel:[0,0,1]
	s_add_u32 s4, s4, s0
	s_addc_u32 s5, s5, 0
	v_lshl_add_u64 v[240:241], s[4:5], 0, v[210:211]
	global_store_dwordx2 v[240:241], v[242:243], off
